# loop-edge edit in both P2 attention tile loops: PV MFMAs accumulate in place, the per-tile phi-register copies (18-24 v_mov per tile) are removed and the epilogue's copies are made once at loop exit
# speedup vs baseline: 1.0088x; 1.0041x over previous
; template <int NQ, int NKF, int MODE> ...
;     ...
;     const unsigned kad0 = kb_ + (unsigned)(krow * 128 + ((gq ^ ksw) << 4)), kad1 = kb_ + (unsigned)(krow * 128 + (((4 + gq) ^ ksw) << 4));
;     bf16x8 kfr[2][NKF];
; #pragma unroll
;     for (int ks = 0; ks < 2; ++ks)
; #pragma unroll
;         for (int kf = 0; kf < NKF; ++kf) AT_DSR128(kfr[ks][kf], (ks ? kad1 : kad0), kf * 2048);
;     ...
;     for (int ks = 0; ks < 2; ++ks)
; #pragma unroll
;         for (int kf = 0; kf < NKF; ++kf)
; #pragma unroll
;             for (int q = 0; q < NQ; ++q) s[q][kf] = mfma16(kfr[ks][kf], qf[q][ks], s[q][kf]);
;     __builtin_amdgcn_sched_barrier(0);
; #pragma unroll
;     for (int t = 0; t < NKF / 2; ++t) {
;         const int ko = koff + 32 * t + 4 * gq, ko2 = ko + 16;
;         const unsigned va = vb_ + (unsigned)(l15 * 128 + (((ko >> 3) ^ vsw) << 4) + ((ko & 4) << 1));
;         const unsigned vh = vb_ + (unsigned)(l15 * 128 + (((ko2 >> 3) ^ vsw) << 4) + ((ko2 & 4) << 1));
; #pragma unroll
;         for (int df = 0; df < 4; ++df) { AT_DSR64(vlo[t][df], va, df * 2048); AT_DSR64(vhi[t][df], vh, df * 2048); }
;     }
;     if (MODE == 2) AT_LW(NKF * 4);
;     bf16x8 pb[NQ][NKF / 2];
; #pragma unroll
;     for (int q = 0; q < NQ; ++q) {
;         unsigned ub = 0; unsigned qm = 0xFFFFFFFFu;
;         if (MODE == 1) ub = (unsigned)((qpos0 + q * 16) - (kpos0 + gq * 4) + 128);
;         if (MODE == 2) qm = ((kpos0 >> q) & 1) ? 0xFFFFFFFFu : 0u;
; #pragma unroll
;         for (int kf = 0; kf < NKF; ++kf)
; #pragma unroll
;             for (int r = 0; r < 4; ++r) {
;                 float xv = __builtin_fmaf(s[q][kf][r], C2, MODE == 2 ? bv[q][kf * 4 + r] : negM2);
;                 if (MODE == 1) { const bool valid = (ub - (unsigned)(kf * 16 + r)) <= 256u; xv = valid ? xv : -1e30f; }
;                 s[q][kf][r] = __builtin_amdgcn_exp2f(xv);
;             }
; #pragma unroll
;         for (int t = 0; t < NKF / 2; ++t) {
;             uint4 w; w.x = pack2(s[q][2 * t][0], s[q][2 * t][1]); w.y = pack2(s[q][2 * t][2], s[q][2 * t][3]);
;             w.z = pack2(s[q][2 * t + 1][0], s[q][2 * t + 1][1]); w.w = pack2(s[q][2 * t + 1][2], s[q][2 * t + 1][3]);
;             if (MODE == 2) { w.x &= nc.cm[0] & qm; w.y &= nc.cm[1] & qm; w.z &= nc.cm[2] & qm; w.w &= nc.cm[3] & qm; }
;             pb[q][t] = __builtin_bit_cast(bf16x8, w);
;         }
;     }
.LBB0_393:
	v_add_u32_e32 v74, v150, v130
	v_add_u32_e32 v70, v74, v131
	v_add_u32_e32 v86, v74, v132
	ds_read_b128 v[58:61], v70 offset:0
	ds_read_b128 v[62:65], v70 offset:0x800
	ds_read_b128 v[66:69], v70 offset:0x1000
	ds_read_b128 v[70:73], v70 offset:0x1800
	ds_read_b128 v[74:77], v86 offset:0
	ds_read_b128 v[78:81], v86 offset:0x800
	ds_read_b128 v[82:85], v86 offset:0x1000
	ds_read_b128 v[86:89], v86 offset:0x1800
	s_nop 0
	s_nop 0
	s_waitcnt lgkmcnt(7)
	v_mfma_f32_16x16x32_bf16 v[90:93], v[58:61], v[2:5], 0
	v_mfma_f32_16x16x32_bf16 v[58:61], v[58:61], v[10:13], 0
	s_waitcnt lgkmcnt(6)
	v_mfma_f32_16x16x32_bf16 v[94:97], v[62:65], v[2:5], 0
	v_mfma_f32_16x16x32_bf16 v[62:65], v[62:65], v[10:13], 0
	s_waitcnt lgkmcnt(5)
	v_mfma_f32_16x16x32_bf16 v[152:155], v[66:69], v[2:5], 0
	v_mfma_f32_16x16x32_bf16 v[66:69], v[66:69], v[10:13], 0
	s_waitcnt lgkmcnt(4)
	v_mfma_f32_16x16x32_bf16 v[156:159], v[70:73], v[2:5], 0
	v_mfma_f32_16x16x32_bf16 v[70:73], v[70:73], v[10:13], 0
	s_waitcnt lgkmcnt(3)
	v_mfma_f32_16x16x32_bf16 v[90:93], v[74:77], v[6:9], v[90:93]
	v_mfma_f32_16x16x32_bf16 v[58:61], v[74:77], v[14:17], v[58:61]
	s_waitcnt lgkmcnt(2)
	v_mfma_f32_16x16x32_bf16 v[74:77], v[78:81], v[6:9], v[94:97]
	v_mfma_f32_16x16x32_bf16 v[62:65], v[78:81], v[14:17], v[62:65]
	s_waitcnt lgkmcnt(1)
	v_mfma_f32_16x16x32_bf16 v[78:81], v[82:85], v[6:9], v[152:155]
	v_mfma_f32_16x16x32_bf16 v[66:69], v[82:85], v[14:17], v[66:69]
	s_waitcnt lgkmcnt(0)
	v_mfma_f32_16x16x32_bf16 v[82:85], v[86:89], v[6:9], v[156:159]
	v_mfma_f32_16x16x32_bf16 v[70:73], v[86:89], v[14:17], v[70:73]
	v_add_u32_e32 v151, v148, v133
	s_nop 0
	v_add_u32_e32 v156, v134, v148
	v_add_u32_e32 v158, v151, v135
	v_add_u32_e32 v172, v147, v148
	v_add_u32_e32 v151, v151, v136
	v_fma_f32 v74, v74, s63, -v113
	ds_read_b64 v[86:87], v156 offset:0
	ds_read_b64 v[88:89], v158 offset:0
	ds_read_b64 v[94:95], v156 offset:0x800
	ds_read_b64 v[96:97], v158 offset:0x800
	ds_read_b64 v[152:153], v156 offset:0x1000
	ds_read_b64 v[154:155], v158 offset:0x1000
	ds_read_b64 v[156:157], v156 offset:0x1800
	ds_read_b64 v[158:159], v158 offset:0x1800
	ds_read_b64 v[160:161], v172 offset:0
	ds_read_b64 v[162:163], v151 offset:0
	ds_read_b64 v[164:165], v172 offset:0x800
	ds_read_b64 v[166:167], v151 offset:0x800
	ds_read_b64 v[168:169], v172 offset:0x1000
	ds_read_b64 v[170:171], v151 offset:0x1000
	ds_read_b64 v[172:173], v172 offset:0x1800
	ds_read_b64 v[174:175], v151 offset:0x1800
	v_exp_f32_e32 v151, v74
	v_fma_f32 v74, v75, s63, -v113
	v_exp_f32_e32 v176, v74
	v_fma_f32 v74, v76, s63, -v113
	v_exp_f32_e32 v177, v74
	v_fma_f32 v74, v77, s63, -v113
	v_exp_f32_e32 v77, v74
	v_fma_f32 v74, v78, s63, -v113
	v_exp_f32_e32 v78, v74
	v_fma_f32 v74, v79, s63, -v113
	v_exp_f32_e32 v79, v74
	v_fma_f32 v74, v80, s63, -v113
	v_exp_f32_e32 v80, v74
	v_fma_f32 v74, v81, s63, -v113
	v_exp_f32_e32 v81, v74
	v_fma_f32 v74, v82, s63, -v113
	v_exp_f32_e32 v82, v74
	v_fma_f32 v74, v83, s63, -v113
	v_fma_f32 v90, v90, s63, -v113
	v_fma_f32 v91, v91, s63, -v113
	v_fma_f32 v92, v92, s63, -v113
	v_fma_f32 v93, v93, s63, -v113
	v_exp_f32_e32 v83, v74
	v_fma_f32 v74, v84, s63, -v113
	v_fma_f32 v58, v58, s63, -v113
	v_fma_f32 v59, v59, s63, -v113
	v_fma_f32 v60, v60, s63, -v113
	v_fma_f32 v61, v61, s63, -v113
	v_fma_f32 v62, v62, s63, -v113
	v_fma_f32 v63, v63, s63, -v113
	v_fma_f32 v64, v64, s63, -v113
	v_fma_f32 v65, v65, s63, -v113
	v_exp_f32_e32 v90, v90
	v_exp_f32_e32 v91, v91
	v_exp_f32_e32 v92, v92
	v_exp_f32_e32 v93, v93
	v_exp_f32_e32 v84, v74
	v_fma_f32 v74, v85, s63, -v113
	v_exp_f32_e32 v58, v58
	v_exp_f32_e32 v59, v59
	v_exp_f32_e32 v60, v60
	v_exp_f32_e32 v61, v61
	v_exp_f32_e32 v62, v62
	v_exp_f32_e32 v63, v63
	v_exp_f32_e32 v64, v64
	v_exp_f32_e32 v65, v65
	v_fma_f32 v66, v66, s63, -v113
	v_fma_f32 v67, v67, s63, -v113
	v_fma_f32 v68, v68, s63, -v113
	v_fma_f32 v69, v69, s63, -v113
	v_fma_f32 v70, v70, s63, -v113
	v_fma_f32 v71, v71, s63, -v113
	v_fma_f32 v72, v72, s63, -v113
	v_fma_f32 v73, v73, s63, -v113
	v_exp_f32_e32 v85, v74
	v_exp_f32_e32 v66, v66
	v_exp_f32_e32 v67, v67
	v_exp_f32_e32 v68, v68
	v_exp_f32_e32 v69, v69
	v_exp_f32_e32 v70, v70
	v_exp_f32_e32 v71, v71
	v_exp_f32_e32 v72, v72
	v_exp_f32_e32 v73, v73
	s_waitcnt lgkmcnt(0)
	v_cvt_pk_bf16_f32 v74, v90, v91
	v_cvt_pk_bf16_f32 v75, v92, v93
	v_cvt_pk_bf16_f32 v76, v151, v176
	v_cvt_pk_bf16_f32 v77, v177, v77
	v_cvt_pk_bf16_f32 v58, v58, v59
	v_cvt_pk_bf16_f32 v59, v60, v61
	v_cvt_pk_bf16_f32 v60, v62, v63
	v_cvt_pk_bf16_f32 v61, v64, v65
	v_cvt_pk_bf16_f32 v176, v78, v79
	v_cvt_pk_bf16_f32 v177, v80, v81
	v_cvt_pk_bf16_f32 v178, v82, v83
	v_cvt_pk_bf16_f32 v179, v84, v85
	v_cvt_pk_bf16_f32 v180, v66, v67
	v_cvt_pk_bf16_f32 v181, v68, v69
	v_cvt_pk_bf16_f32 v182, v70, v71
	v_cvt_pk_bf16_f32 v183, v72, v73
	s_mov_b32 s38, s36
	s_mov_b32 s39, s36
	s_mov_b32 s37, s36
	v_mov_b64_e32 v[64:65], s[38:39]
	v_mov_b64_e32 v[62:63], s[36:37]
	v_mfma_f32_16x16x32_bf16 v[46:49], v[86:89], v[74:77], v[46:49]
	s_nop 0
	v_mfma_f32_16x16x32_bf16 v[50:53], v[62:65], v[74:77], v[50:53]
	v_mfma_f32_16x16x32_bf16 v[54:57], v[62:65], v[58:61], v[54:57]
	v_mfma_f32_16x16x32_bf16 v[42:45], v[86:89], v[58:61], v[42:45]
	v_mfma_f32_16x16x32_bf16 v[38:41], v[94:97], v[74:77], v[38:41]
	v_mfma_f32_16x16x32_bf16 v[34:37], v[94:97], v[58:61], v[34:37]
	v_mfma_f32_16x16x32_bf16 v[30:33], v[152:155], v[74:77], v[30:33]
	v_mfma_f32_16x16x32_bf16 v[26:29], v[152:155], v[58:61], v[26:29]
	v_mfma_f32_16x16x32_bf16 v[22:25], v[156:159], v[74:77], v[22:25]
	v_mfma_f32_16x16x32_bf16 v[18:21], v[156:159], v[58:61], v[18:21]
	v_mfma_f32_16x16x32_bf16 v[50:53], v[62:65], v[176:179], v[50:53]
	v_mfma_f32_16x16x32_bf16 v[54:57], v[62:65], v[180:183], v[54:57]
	v_mfma_f32_16x16x32_bf16 v[46:49], v[160:163], v[176:179], v[46:49]
	v_mfma_f32_16x16x32_bf16 v[42:45], v[160:163], v[180:183], v[42:45]
	v_mfma_f32_16x16x32_bf16 v[38:41], v[164:167], v[176:179], v[38:41]
	v_mfma_f32_16x16x32_bf16 v[34:37], v[164:167], v[180:183], v[34:37]
	v_mfma_f32_16x16x32_bf16 v[30:33], v[168:171], v[176:179], v[30:33]
	v_mfma_f32_16x16x32_bf16 v[26:29], v[168:171], v[180:183], v[26:29]
	v_mfma_f32_16x16x32_bf16 v[22:25], v[172:175], v[176:179], v[22:25]
	v_mfma_f32_16x16x32_bf16 v[18:21], v[172:175], v[180:183], v[18:21]
	s_cbranch_execnz .LBB0_392
; template <int NQ, int NKF, int MODE> ...
;     ...
;         for (int q = 0; q < NQ; ++q) {
;             int drq = qpos0 - q; drq = drq < 0 ? 0 : (drq > 14 ? 14 : drq);
;             const unsigned ba = nc.blane + (unsigned)(drq * 256);
; #pragma unroll
;             for (int kf = 0; kf < NKF; ++kf)
; #pragma unroll
;                 for (int r = 0; r < 4; ++r) AT_DSR32(bv[q][kf * 4 + r], ba, (kf * 16 + r) * 4);
;         }
;     }
;     const int vsw = (l15 >> 1) & 7;
;     i32x2 vlo[NKF / 2][4], vhi[NKF / 2][4];
; #pragma unroll
;     for (int q = 0; q < NQ; ++q)
; #pragma unroll
;         for (int kf = 0; kf < NKF; ++kf) s[q][kf] = (f32x4){0.f, 0.f, 0.f, 0.f};
;     if (MODE == 2) AT_LW((NQ * NKF * 4 > 15 ? 15 : NQ * NKF * 4)); else AT_LW(0);
; #pragma unroll
;     for (int ks = 0; ks < 2; ++ks)
; #pragma unroll
;         for (int kf = 0; kf < NKF; ++kf)
; #pragma unroll
;             for (int q = 0; q < NQ; ++q) s[q][kf] = mfma16(kfr[ks][kf], qf[q][ks], s[q][kf]);
;     __builtin_amdgcn_sched_barrier(0);
; #pragma unroll
;     for (int t = 0; t < NKF / 2; ++t) {
;         const int ko = koff + 32 * t + 4 * gq, ko2 = ko + 16;
;         const unsigned va = vb_ + (unsigned)(l15 * 128 + (((ko >> 3) ^ vsw) << 4) + ((ko & 4) << 1));
;         const unsigned vh = vb_ + (unsigned)(l15 * 128 + (((ko2 >> 3) ^ vsw) << 4) + ((ko2 & 4) << 1));
; #pragma unroll
;         for (int df = 0; df < 4; ++df) { AT_DSR64(vlo[t][df], va, df * 2048); AT_DSR64(vhi[t][df], vh, df * 2048); }
;     }
;     if (MODE == 2) AT_LW(NKF * 4);
;     bf16x8 pb[NQ][NKF / 2];
; #pragma unroll
;     for (int q = 0; q < NQ; ++q) {
;         unsigned ub = 0; unsigned qm = 0xFFFFFFFFu;
;         if (MODE == 1) ub = (unsigned)((qpos0 + q * 16) - (kpos0 + gq * 4) + 128);
;         if (MODE == 2) qm = ((kpos0 >> q) & 1) ? 0xFFFFFFFFu : 0u;
; #pragma unroll
;         for (int kf = 0; kf < NKF; ++kf)
; #pragma unroll
;             for (int r = 0; r < 4; ++r) {
;                 float xv = __builtin_fmaf(s[q][kf][r], C2, MODE == 2 ? bv[q][kf * 4 + r] : negM2);
;                 if (MODE == 1) { const bool valid = (ub - (unsigned)(kf * 16 + r)) <= 256u; xv = valid ? xv : -1e30f; }
;                 s[q][kf][r] = __builtin_amdgcn_exp2f(xv);
;             }
; #pragma unroll
;         for (int t = 0; t < NKF / 2; ++t) {
.LBB0_394:
	v_add_u32_e32 v58, 0xffffe1c0, v149
	v_ashrrev_i32_e32 v58, 6, v58
	v_sub_u32_e32 v59, v58, v101
	s_nop 3
	v_add_u32_e32 v74, 7, v59
	v_med3_i32 v75, v74, 0, 14
	v_max_i32_e32 v74, 1, v74
	v_add_u32_e32 v66, v150, v141
	v_add_u32_e32 v74, -1, v74
	v_cmp_ge_i32_e32 vcc, v58, v137
	v_cmp_lt_i32_e64 s[0:1], v58, v139
	v_add_u32_e32 v62, v66, v142
	v_add_u32_e32 v70, v66, v143
	v_min_u32_e32 v74, 14, v74
	s_and_b64 s[0:1], vcc, s[0:1]
	v_cmp_ge_i32_e32 vcc, v58, v138
	v_cmp_lt_i32_e64 s[6:7], v58, v140
	ds_read_b128 v[58:61], v62 offset:0
	ds_read_b128 v[62:65], v62 offset:0x800
	ds_read_b128 v[66:69], v70 offset:0
	ds_read_b128 v[70:73], v70 offset:0x800
	v_lshl_add_u32 v75, v75, 8, v129
	ds_read_b32 v82, v75 offset:0
	ds_read_b32 v83, v75 offset:4
	ds_read_b32 v84, v75 offset:8
	ds_read_b32 v85, v75 offset:12
	ds_read_b32 v86, v75 offset:64
	ds_read_b32 v87, v75 offset:0x44
	ds_read_b32 v88, v75 offset:0x48
	ds_read_b32 v89, v75 offset:0x4c
	v_lshl_add_u32 v74, v74, 8, v129
	ds_read_b32 v152, v74 offset:0
	ds_read_b32 v153, v74 offset:4
	ds_read_b32 v154, v74 offset:8
	ds_read_b32 v155, v74 offset:12
	ds_read_b32 v156, v74 offset:64
	ds_read_b32 v157, v74 offset:0x44
	ds_read_b32 v158, v74 offset:0x48
	ds_read_b32 v159, v74 offset:0x4c
	s_waitcnt lgkmcnt(15)
	s_and_b64 vcc, vcc, s[6:7]
	v_mfma_f32_16x16x32_bf16 v[74:77], v[58:61], v[2:5], 0
	v_mfma_f32_16x16x32_bf16 v[58:61], v[58:61], v[10:13], 0
	v_mfma_f32_16x16x32_bf16 v[78:81], v[62:65], v[2:5], 0
	v_mfma_f32_16x16x32_bf16 v[62:65], v[62:65], v[10:13], 0
	v_mfma_f32_16x16x32_bf16 v[74:77], v[66:69], v[6:9], v[74:77]
	v_mfma_f32_16x16x32_bf16 v[58:61], v[66:69], v[14:17], v[58:61]
	v_mfma_f32_16x16x32_bf16 v[66:69], v[70:73], v[6:9], v[78:81]
	v_mfma_f32_16x16x32_bf16 v[62:65], v[70:73], v[14:17], v[62:65]
	v_add_u32_e32 v70, v148, v145
	s_nop 1
	v_add_u32_e32 v78, v70, v144
	v_add_u32_e32 v79, v70, v146
	ds_read_b64 v[70:71], v78 offset:0
	ds_read_b64 v[72:73], v79 offset:0
	ds_read_b64 v[90:91], v78 offset:0x800
	ds_read_b64 v[92:93], v79 offset:0x800
	ds_read_b64 v[94:95], v78 offset:0x1000
	ds_read_b64 v[96:97], v79 offset:0x1000
	ds_read_b64 v[148:149], v78 offset:0x1800
	ds_read_b64 v[150:151], v79 offset:0x1800
	s_waitcnt lgkmcnt(8)
	v_fmac_f32_e32 v82, 0x3e38aa3b, v74
	v_fmac_f32_e32 v83, 0x3e38aa3b, v75
	v_fmac_f32_e32 v86, 0x3e38aa3b, v66
	v_fmac_f32_e32 v87, 0x3e38aa3b, v67
	v_fmac_f32_e32 v88, 0x3e38aa3b, v68
	v_fmac_f32_e32 v89, 0x3e38aa3b, v69
	v_exp_f32_e32 v74, v82
	v_exp_f32_e32 v75, v83
	v_fmac_f32_e32 v84, 0x3e38aa3b, v76
	v_fmac_f32_e32 v85, 0x3e38aa3b, v77
	v_exp_f32_e32 v66, v86
	v_exp_f32_e32 v67, v87
	v_exp_f32_e32 v68, v88
	v_exp_f32_e32 v69, v89
	v_fmac_f32_e32 v152, 0x3e38aa3b, v58
	v_fmac_f32_e32 v153, 0x3e38aa3b, v59
	v_fmac_f32_e32 v154, 0x3e38aa3b, v60
	v_fmac_f32_e32 v155, 0x3e38aa3b, v61
	v_fmac_f32_e32 v156, 0x3e38aa3b, v62
	v_fmac_f32_e32 v157, 0x3e38aa3b, v63
	v_exp_f32_e32 v76, v84
	v_exp_f32_e32 v77, v85
	v_exp_f32_e32 v58, v152
	v_exp_f32_e32 v59, v153
	v_exp_f32_e32 v60, v154
	v_exp_f32_e32 v61, v155
	v_exp_f32_e32 v62, v156
	v_exp_f32_e32 v63, v157
	v_fmac_f32_e32 v158, 0x3e38aa3b, v64
	v_fmac_f32_e32 v159, 0x3e38aa3b, v65
	v_cvt_pk_bf16_f32 v74, v74, v75
	v_cvt_pk_bf16_f32 v66, v66, v67
	v_cvt_pk_bf16_f32 v67, v68, v69
	v_cndmask_b32_e64 v68, 0, v125, s[0:1]
	v_exp_f32_e32 v64, v158
	v_exp_f32_e32 v65, v159
	v_cvt_pk_bf16_f32 v75, v76, v77
	v_and_b32_e32 v74, v68, v74
	v_cndmask_b32_e64 v68, 0, v126, s[0:1]
	v_cvt_pk_bf16_f32 v58, v58, v59
	v_cvt_pk_bf16_f32 v59, v60, v61
	v_cvt_pk_bf16_f32 v60, v62, v63
	v_cndmask_b32_e32 v62, 0, v125, vcc
	v_and_b32_e32 v75, v68, v75
	v_cndmask_b32_e64 v68, 0, v127, s[0:1]
	v_and_b32_e32 v152, v62, v58
	v_cndmask_b32_e32 v58, 0, v126, vcc
	s_waitcnt lgkmcnt(0)
	v_and_b32_e32 v76, v68, v66
	v_cndmask_b32_e64 v66, 0, v128, s[0:1]
	v_and_b32_e32 v153, v58, v59
	v_cndmask_b32_e32 v58, 0, v127, vcc
	v_and_b32_e32 v77, v66, v67
	v_cvt_pk_bf16_f32 v61, v64, v65
	v_and_b32_e32 v154, v58, v60
	v_cndmask_b32_e32 v58, 0, v128, vcc
	v_and_b32_e32 v155, v58, v61
	s_mov_b32 s38, s36
	s_mov_b32 s39, s36
	s_mov_b32 s37, s36
	v_mov_b64_e32 v[60:61], s[38:39]
	v_mov_b64_e32 v[58:59], s[36:37]
	v_mfma_f32_16x16x32_bf16 v[46:49], v[70:73], v[74:77], v[46:49]
	s_nop 0
	v_mfma_f32_16x16x32_bf16 v[50:53], v[58:61], v[74:77], v[50:53]
	v_mfma_f32_16x16x32_bf16 v[54:57], v[58:61], v[152:155], v[54:57]
	v_mfma_f32_16x16x32_bf16 v[42:45], v[70:73], v[152:155], v[42:45]
	v_mfma_f32_16x16x32_bf16 v[38:41], v[90:93], v[74:77], v[38:41]
	v_mfma_f32_16x16x32_bf16 v[34:37], v[90:93], v[152:155], v[34:37]
	v_mfma_f32_16x16x32_bf16 v[30:33], v[94:97], v[74:77], v[30:33]
	v_mfma_f32_16x16x32_bf16 v[26:29], v[94:97], v[152:155], v[26:29]
	v_mfma_f32_16x16x32_bf16 v[22:25], v[148:151], v[74:77], v[22:25]
	v_mfma_f32_16x16x32_bf16 v[18:21], v[148:151], v[152:155], v[18:21]
	s_add_i32 s8, s8, 64
	s_add_i32 s26, s26, 1
	s_cmpk_eq_i32 s8, 0x2180
	s_cbranch_scc1 .LBB0_396
; template <bool ISA>
; __device__ __forceinline__ void attn_unit(const Params& p, unsigned char* smem, int b, int hh, int blk) {
;     ...
; #pragma unroll
;     for (int q = 0; q < NQ; ++q) {
;         const float inv = 1.0f / osum[q][0];
;         float ssq = 0.f;
; #pragma unroll
;         for (int df = 0; df < 4; ++df) { o[q][df] *= inv; ssq += o[q][df][0] * o[q][df][0] + o[q][df][1] * o[q][df][1] + o[q][df][2] * o[q][df][2] + o[q][df][3] * o[q][df][3]; }
;         ssq += __shfl_xor(ssq, 16); ssq += __shfl_xor(ssq, 32);
;         const size_t lr = (size_t)b * SEQ + qt0 + q * QSTR + l15;
;         if (gq == 0) p.osq[lr * 16 + (ISA ? hh : 8 + hh)] = ssq;
.LBB0_395:
	s_cmpk_eq_i32 s8, 0x2140
	s_mov_b64 s[0:1], -1
	s_cbranch_scc0 .LBB0_385
	s_branch .LBB0_386
.LBB0_396:
	s_nop 7
	v_mov_b64_e32 v[74:75], v[18:19]
	v_mov_b64_e32 v[94:95], v[22:23]
	v_mov_b64_e32 v[70:71], v[26:27]
	v_mov_b64_e32 v[90:91], v[30:31]
	v_mov_b64_e32 v[66:67], v[34:35]
	v_mov_b64_e32 v[86:87], v[38:39]
	v_mov_b64_e32 v[62:63], v[42:43]
	v_mov_b64_e32 v[82:83], v[46:47]
	v_mov_b64_e32 v[76:77], v[20:21]
	v_mov_b64_e32 v[96:97], v[24:25]
	v_mov_b64_e32 v[72:73], v[28:29]
	v_mov_b64_e32 v[92:93], v[32:33]
	v_mov_b64_e32 v[68:69], v[36:37]
	v_mov_b64_e32 v[88:89], v[40:41]
	v_mov_b64_e32 v[64:65], v[44:45]
	v_mov_b64_e32 v[84:85], v[48:49]
	v_mov_b32_e32 v78, v50
	v_mov_b32_e32 v79, v51
	v_mov_b32_e32 v80, v52
	v_mov_b32_e32 v81, v53
	v_mov_b32_e32 v58, v54
	v_mov_b32_e32 v59, v55
	v_mov_b32_e32 v60, v56
	v_mov_b32_e32 v61, v57
	v_and_b32_e32 v3, 64, v214
	v_add_u32_e32 v5, 64, v3
	v_div_scale_f32 v3, s[0:1], v78, v78, 1.0
	v_rcp_f32_e32 v4, v3
	v_xor_b32_e32 v2, 16, v214
	v_cmp_lt_i32_e32 vcc, v2, v5
	v_xor_b32_e32 v20, 32, v214
	s_lshl_b32 s0, s24, 13
	v_cndmask_b32_e32 v2, v214, v2, vcc
	v_lshlrev_b32_e32 v22, 2, v2
	v_fma_f32 v2, -v3, v4, 1.0
	v_fmac_f32_e32 v4, v2, v4
	v_div_scale_f32 v2, vcc, 1.0, v78, 1.0
	v_mul_f32_e32 v6, v2, v4
	v_fma_f32 v7, -v3, v6, v2
	v_fmac_f32_e32 v6, v7, v4
	v_fma_f32 v2, -v3, v6, v2
	v_div_fmas_f32 v2, v2, v4, v6
	v_div_fixup_f32 v4, v2, v78, 1.0
	v_pk_mul_f32 v[18:19], v[82:83], v[4:5] op_sel_hi:[1,0]
	v_pk_mul_f32 v[16:17], v[86:87], v[4:5] op_sel_hi:[1,0]
	v_mul_f32_e32 v2, v19, v19
	v_mul_f32_e32 v3, v17, v17
	v_pk_mul_f32 v[14:15], v[84:85], v[4:5] op_sel_hi:[1,0]
	v_fmac_f32_e32 v2, v18, v18
	v_pk_mul_f32 v[8:9], v[88:89], v[4:5] op_sel_hi:[1,0]
	v_fmac_f32_e32 v3, v16, v16
	v_fmac_f32_e32 v2, v14, v14
	v_fmac_f32_e32 v3, v8, v8
	v_fmac_f32_e32 v2, v15, v15
	v_fmac_f32_e32 v3, v9, v9
	v_pk_mul_f32 v[12:13], v[90:91], v[4:5] op_sel_hi:[1,0]
	v_add_f32_e32 v2, v2, v3
	v_mul_f32_e32 v3, v13, v13
	v_pk_mul_f32 v[6:7], v[92:93], v[4:5] op_sel_hi:[1,0]
	v_fmac_f32_e32 v3, v12, v12
	v_fmac_f32_e32 v3, v6, v6
	v_fmac_f32_e32 v3, v7, v7
	v_pk_mul_f32 v[10:11], v[94:95], v[4:5] op_sel_hi:[1,0]
	v_add_f32_e32 v21, v3, v2
	v_pk_mul_f32 v[2:3], v[96:97], v[4:5] op_sel_hi:[1,0]
	v_mul_f32_e32 v4, v11, v11
	v_fmac_f32_e32 v4, v10, v10
	v_fmac_f32_e32 v4, v2, v2
	v_fmac_f32_e32 v4, v3, v3
	v_add_f32_e32 v4, v4, v21
	ds_bpermute_b32 v21, v22, v4
	v_cmp_lt_i32_e32 vcc, v20, v5
	s_mov_b32 s1, s77
	v_ashrrev_i32_e32 v101, 31, v100
	v_cndmask_b32_e32 v5, v214, v20, vcc
	v_lshlrev_b32_e32 v23, 2, v5
	s_waitcnt lgkmcnt(0)
	v_add_f32_e32 v20, v4, v21
	ds_bpermute_b32 v21, v23, v20
	v_lshl_add_u64 v[4:5], v[100:101], 0, s[0:1]
	v_or_b32_e32 v4, v4, v112
	v_cmp_gt_u32_e64 s[0:1], 16, v103
	s_and_saveexec_b64 s[6:7], s[0:1]
	s_cbranch_execz .LBB0_398
	s_waitcnt lgkmcnt(0)
	v_add_f32_e32 v24, v20, v21
	v_lshlrev_b64 v[20:21], 6, v[4:5]
	v_lshl_add_u64 v[20:21], s[70:71], 0, v[20:21]
	s_lshl_b32 s8, s23, 2
	s_mov_b32 s9, s77
	v_lshl_add_u64 v[20:21], v[20:21], 0, s[8:9]
	global_store_dword v[20:21], v24, off

; template <bool ISA>
; __device__ __forceinline__ void attn_unit(const Params& p, unsigned char* smem, int b, int hh, int blk) {
;     ...
; #pragma unroll 1
;     for (int ti = 0; ti < ntile; ++ti) {
;         if (ti + 1 < ntile) asm volatile("s_waitcnt vmcnt(4)" ::: "memory"); else asm volatile("s_waitcnt vmcnt(0)" ::: "memory");
;         asm volatile("s_waitcnt lgkmcnt(0)" ::: "memory"); __builtin_amdgcn_s_barrier(); asm volatile("" ::: "memory");
;         if (ti + 2 < ntile) ADMA(ti + 2);
.LBB0_404:
	s_or_b64 exec, exec, s[60:61]
	s_and_b64 s[0:1], exec, vcc
	s_or_b64 s[82:83], s[0:1], s[82:83]
	v_subrev_u32_e32 v110, 64, v110
	v_add_u32_e32 v86, 64, v86
	s_addk_i32 s73, 0x2000
	s_add_i32 s72, s72, 1
	s_mov_b32 s8, s30
	s_andn2_b64 exec, exec, s[82:83]
	s_cbranch_execz .LBB0_420

; template <int NQ, int NKF, int MODE> ...
;     ...
;     for (int ks = 0; ks < 2; ++ks)
; #pragma unroll
;         for (int kf = 0; kf < NKF; ++kf)
; #pragma unroll
;             for (int q = 0; q < NQ; ++q) s[q][kf] = mfma16(kfr[ks][kf], qf[q][ks], s[q][kf]);
;     __builtin_amdgcn_sched_barrier(0);
; #pragma unroll
;     for (int t = 0; t < NKF / 2; ++t) {
;         const int ko = koff + 32 * t + 4 * gq, ko2 = ko + 16;
;         const unsigned va = vb_ + (unsigned)(l15 * 128 + (((ko >> 3) ^ vsw) << 4) + ((ko & 4) << 1));
;         const unsigned vh = vb_ + (unsigned)(l15 * 128 + (((ko2 >> 3) ^ vsw) << 4) + ((ko2 & 4) << 1));
; #pragma unroll
;         for (int df = 0; df < 4; ++df) { AT_DSR64(vlo[t][df], va, df * 2048); AT_DSR64(vhi[t][df], vh, df * 2048); }
;     }
;     if (MODE == 2) AT_LW(NKF * 4);
;     bf16x8 pb[NQ][NKF / 2];
; #pragma unroll
;     for (int q = 0; q < NQ; ++q) {
;         unsigned ub = 0; unsigned qm = 0xFFFFFFFFu;
;         if (MODE == 1) ub = (unsigned)((qpos0 + q * 16) - (kpos0 + gq * 4) + 128);
;         if (MODE == 2) qm = ((kpos0 >> q) & 1) ? 0xFFFFFFFFu : 0u;
; #pragma unroll
;         for (int kf = 0; kf < NKF; ++kf)
; #pragma unroll
;             for (int r = 0; r < 4; ++r) {
;                 float xv = __builtin_fmaf(s[q][kf][r], C2, MODE == 2 ? bv[q][kf * 4 + r] : negM2);
;                 if (MODE == 1) { const bool valid = (ub - (unsigned)(kf * 16 + r)) <= 256u; xv = valid ? xv : -1e30f; }
;                 s[q][kf][r] = __builtin_amdgcn_exp2f(xv);
;             }
; #pragma unroll
;         for (int t = 0; t < NKF / 2; ++t) {
;             uint4 w; w.x = pack2(s[q][2 * t][0], s[q][2 * t][1]); w.y = pack2(s[q][2 * t][2], s[q][2 * t][3]);
;             w.z = pack2(s[q][2 * t + 1][0], s[q][2 * t + 1][1]); w.w = pack2(s[q][2 * t + 1][2], s[q][2 * t + 1][3]);
;             if (MODE == 2) { w.x &= nc.cm[0] & qm; w.y &= nc.cm[1] & qm; w.z &= nc.cm[2] & qm; w.w &= nc.cm[3] & qm; }
;             pb[q][t] = __builtin_bit_cast(bf16x8, w);
;         }
;     }
;     const bf16x8 ones = {0x3F80, 0x3F80, 0x3F80, 0x3F80, 0x3F80, 0x3F80, 0x3F80, 0x3F80};
;     AT_LW(0);
; #pragma unroll
;     for (int t = 0; t < NKF / 2; ++t) {
; #pragma unroll
;         for (int q = 0; q < NQ; ++q) osum[q] = mfma16(ones, pb[q][t], osum[q]);
; #pragma unroll
;         for (int df = 0; df < 4; ++df) {
.LBB0_411:
	s_or_b64 exec, exec, s[6:7]
	s_mul_hi_u32 s0, s8, 0xaaaaaaab
	s_lshr_b32 s0, s0, 1
	s_mulk_i32 s0, 0x6000
	v_subrev_u32_e32 v127, s0, v111
	v_subrev_u32_e32 v129, s0, v113
	v_subrev_u32_e32 v128, s0, v125
	v_subrev_u32_e32 v130, s0, v126
	v_subrev_u32_e32 v131, s0, v104
	v_subrev_u32_e32 v132, s0, v103
	v_cmp_ge_u32_e64 s[0:1], s8, v101
	s_and_saveexec_b64 s[6:7], s[0:1]
	s_xor_b64 s[0:1], exec, s[6:7]
	s_cbranch_execz .LBB0_413
	v_add_u32_e32 v156, s73, v112
	v_add_u32_e32 v70, v156, v132
	ds_read_b128 v[58:61], v70 offset:0
	ds_read_b128 v[62:65], v70 offset:0x800
	ds_read_b128 v[66:69], v70 offset:0x1000
	ds_read_b128 v[70:73], v70 offset:0x1800
	v_add_u32_e32 v131, v156, v131
	ds_read_b128 v[74:77], v131 offset:0
	ds_read_b128 v[78:81], v131 offset:0x800
	ds_read_b128 v[132:135], v131 offset:0x1000
	ds_read_b128 v[136:139], v131 offset:0x1800
	s_nop 0
	s_waitcnt lgkmcnt(7)
	v_mfma_f32_16x16x32_bf16 v[140:143], v[58:61], v[14:17], 0
	v_mfma_f32_16x16x32_bf16 v[58:61], v[58:61], v[6:9], 0
	s_waitcnt lgkmcnt(6)
	v_mfma_f32_16x16x32_bf16 v[144:147], v[62:65], v[14:17], 0
	v_mfma_f32_16x16x32_bf16 v[62:65], v[62:65], v[6:9], 0
	s_waitcnt lgkmcnt(5)
	v_mfma_f32_16x16x32_bf16 v[148:151], v[66:69], v[14:17], 0
	v_mfma_f32_16x16x32_bf16 v[66:69], v[66:69], v[6:9], 0
	s_waitcnt lgkmcnt(4)
	v_mfma_f32_16x16x32_bf16 v[152:155], v[70:73], v[14:17], 0
	v_mfma_f32_16x16x32_bf16 v[70:73], v[70:73], v[6:9], 0
	s_waitcnt lgkmcnt(3)
	v_mfma_f32_16x16x32_bf16 v[140:143], v[74:77], v[2:5], v[140:143]
	v_mfma_f32_16x16x32_bf16 v[58:61], v[74:77], v[10:13], v[58:61]
	s_waitcnt lgkmcnt(2)
	v_mfma_f32_16x16x32_bf16 v[74:77], v[78:81], v[2:5], v[144:147]
	v_mfma_f32_16x16x32_bf16 v[62:65], v[78:81], v[10:13], v[62:65]
	s_waitcnt lgkmcnt(1)
	v_mfma_f32_16x16x32_bf16 v[78:81], v[132:135], v[2:5], v[148:151]
	v_mfma_f32_16x16x32_bf16 v[66:69], v[132:135], v[10:13], v[66:69]
	s_waitcnt lgkmcnt(0)
	v_mfma_f32_16x16x32_bf16 v[132:135], v[136:139], v[2:5], v[152:155]
	v_mfma_f32_16x16x32_bf16 v[70:73], v[136:139], v[10:13], v[70:73]
	v_add_u32_e32 v129, v156, v129
	v_add_u32_e32 v130, v156, v130
	v_add_u32_e32 v127, v156, v127
	v_fma_f32 v74, v74, s63, -v100
	ds_read_b64 v[136:137], v129 offset:0
	ds_read_b64 v[138:139], v130 offset:0
	ds_read_b64 v[144:145], v129 offset:0x800
	ds_read_b64 v[146:147], v130 offset:0x800
	ds_read_b64 v[148:149], v129 offset:0x1000
	ds_read_b64 v[150:151], v130 offset:0x1000
	ds_read_b64 v[152:153], v129 offset:0x1800
	ds_read_b64 v[154:155], v130 offset:0x1800
	v_add_u32_e32 v166, v156, v128
	ds_read_b64 v[128:129], v127 offset:0
	ds_read_b64 v[130:131], v166 offset:0
	ds_read_b64 v[156:157], v127 offset:0x800
	ds_read_b64 v[158:159], v166 offset:0x800
	ds_read_b64 v[160:161], v127 offset:0x1000
	ds_read_b64 v[162:163], v166 offset:0x1000
	ds_read_b64 v[164:165], v127 offset:0x1800
	v_fma_f32 v127, v140, s63, -v100
	v_fma_f32 v140, v141, s63, -v100
	v_fma_f32 v141, v142, s63, -v100
	v_fma_f32 v142, v143, s63, -v100
	v_exp_f32_e32 v143, v74
	v_fma_f32 v74, v75, s63, -v100
	v_exp_f32_e32 v168, v74
	v_fma_f32 v74, v76, s63, -v100
	v_exp_f32_e32 v169, v74
	v_fma_f32 v74, v77, s63, -v100
	v_exp_f32_e32 v77, v74
	v_fma_f32 v74, v78, s63, -v100
	v_exp_f32_e32 v78, v74
	v_fma_f32 v74, v79, s63, -v100
	v_exp_f32_e32 v79, v74
	v_fma_f32 v74, v80, s63, -v100
	v_exp_f32_e32 v80, v74
	v_fma_f32 v74, v81, s63, -v100
	v_exp_f32_e32 v81, v74
	v_fma_f32 v74, v132, s63, -v100
	v_exp_f32_e32 v127, v127
	v_exp_f32_e32 v140, v140
	v_exp_f32_e32 v132, v74
	v_fma_f32 v74, v133, s63, -v100
	v_exp_f32_e32 v133, v74
	v_fma_f32 v74, v134, s63, -v100
	v_exp_f32_e32 v134, v74
	v_fma_f32 v74, v135, s63, -v100
	v_fma_f32 v70, v70, s63, -v100
	v_exp_f32_e32 v135, v74
	v_cvt_pk_bf16_f32 v74, v127, v140
	v_exp_f32_e32 v127, v70
	v_fma_f32 v70, v71, s63, -v100
	v_cvt_pk_bf16_f32 v78, v78, v79
	v_cvt_pk_bf16_f32 v79, v80, v81
	v_cvt_pk_bf16_f32 v80, v132, v133
	v_fma_f32 v58, v58, s63, -v100
	v_fma_f32 v59, v59, s63, -v100
	v_fma_f32 v60, v60, s63, -v100
	v_fma_f32 v61, v61, s63, -v100
	v_fma_f32 v62, v62, s63, -v100
	v_fma_f32 v63, v63, s63, -v100
	v_fma_f32 v64, v64, s63, -v100
	v_fma_f32 v65, v65, s63, -v100
	v_exp_f32_e32 v132, v70
	v_fma_f32 v70, v72, s63, -v100
	v_exp_f32_e32 v58, v58
	v_exp_f32_e32 v59, v59
	v_exp_f32_e32 v60, v60
	v_exp_f32_e32 v61, v61
	v_exp_f32_e32 v62, v62
	v_exp_f32_e32 v63, v63
	v_exp_f32_e32 v64, v64
	v_exp_f32_e32 v65, v65
	v_fma_f32 v66, v66, s63, -v100
	v_fma_f32 v67, v67, s63, -v100
	v_fma_f32 v68, v68, s63, -v100
	v_fma_f32 v69, v69, s63, -v100
	v_exp_f32_e32 v133, v70
	v_fma_f32 v70, v73, s63, -v100
	v_exp_f32_e32 v141, v141
	v_exp_f32_e32 v142, v142
	v_exp_f32_e32 v66, v66
	v_exp_f32_e32 v67, v67
	v_exp_f32_e32 v68, v68
	v_exp_f32_e32 v69, v69
	v_exp_f32_e32 v73, v70
	ds_read_b64 v[166:167], v166 offset:0x1800
	s_waitcnt lgkmcnt(0)
	v_cvt_pk_bf16_f32 v58, v58, v59
	v_cvt_pk_bf16_f32 v59, v60, v61
	v_cvt_pk_bf16_f32 v60, v62, v63
	v_cvt_pk_bf16_f32 v61, v64, v65
	v_cvt_pk_bf16_f32 v75, v141, v142
	v_cvt_pk_bf16_f32 v76, v143, v168
	v_cvt_pk_bf16_f32 v77, v169, v77
	v_cvt_pk_bf16_f32 v81, v134, v135
	v_cvt_pk_bf16_f32 v70, v66, v67
	v_cvt_pk_bf16_f32 v71, v68, v69
	v_cvt_pk_bf16_f32 v72, v127, v132
	v_cvt_pk_bf16_f32 v73, v133, v73
	s_mov_b32 s38, s36
	s_mov_b32 s39, s36
	s_mov_b32 s37, s36
	v_mov_b64_e32 v[64:65], s[38:39]
	v_mov_b64_e32 v[62:63], s[36:37]
	v_mfma_f32_16x16x32_bf16 v[54:57], v[136:139], v[74:77], v[54:57]
	s_nop 0
	v_mfma_f32_16x16x32_bf16 v[38:41], v[62:65], v[74:77], v[38:41]
	v_mfma_f32_16x16x32_bf16 v[26:29], v[62:65], v[58:61], v[26:29]
	v_mfma_f32_16x16x32_bf16 v[50:53], v[136:139], v[58:61], v[50:53]
	v_mfma_f32_16x16x32_bf16 v[46:49], v[144:147], v[74:77], v[46:49]
	v_mfma_f32_16x16x32_bf16 v[22:25], v[144:147], v[58:61], v[22:25]
	v_mfma_f32_16x16x32_bf16 v[42:45], v[148:151], v[74:77], v[42:45]
	v_mfma_f32_16x16x32_bf16 v[18:21], v[148:151], v[58:61], v[18:21]
	v_mfma_f32_16x16x32_bf16 v[34:37], v[152:155], v[74:77], v[34:37]
	v_mfma_f32_16x16x32_bf16 v[30:33], v[152:155], v[58:61], v[30:33]
	v_mfma_f32_16x16x32_bf16 v[38:41], v[62:65], v[78:81], v[38:41]
	v_mfma_f32_16x16x32_bf16 v[26:29], v[62:65], v[70:73], v[26:29]
	v_mfma_f32_16x16x32_bf16 v[54:57], v[128:131], v[78:81], v[54:57]
	v_mfma_f32_16x16x32_bf16 v[50:53], v[128:131], v[70:73], v[50:53]
	v_mfma_f32_16x16x32_bf16 v[46:49], v[156:159], v[78:81], v[46:49]
	v_mfma_f32_16x16x32_bf16 v[22:25], v[156:159], v[70:73], v[22:25]
	v_mfma_f32_16x16x32_bf16 v[42:45], v[160:163], v[78:81], v[42:45]
	v_mfma_f32_16x16x32_bf16 v[18:21], v[160:163], v[70:73], v[18:21]
	v_mfma_f32_16x16x32_bf16 v[34:37], v[164:167], v[78:81], v[34:37]
	v_mfma_f32_16x16x32_bf16 v[30:33], v[164:167], v[70:73], v[30:33]
; __device__ __forceinline__ f32x4 mfma16(bf16x8 a, bf16x8 b, f32x4 c) { return __builtin_amdgcn_mfma_f32_16x16x32_bf16(a, b, c, 0, 0, 0); }
; #define AT_DSR64(dst, addr, off) asm volatile("ds_read_b64 %0, %1 offset:%2" : "=v"(dst) : "v"(addr), "i"(off))
; template <int NQ, int NKF, int MODE> ...
;     ...
;     for (int ks = 0; ks < 2; ++ks)
; #pragma unroll
;         for (int kf = 0; kf < NKF; ++kf)
; #pragma unroll
;             for (int q = 0; q < NQ; ++q) s[q][kf] = mfma16(kfr[ks][kf], qf[q][ks], s[q][kf]);
;     __builtin_amdgcn_sched_barrier(0);
; #pragma unroll
;     for (int t = 0; t < NKF / 2; ++t) {
;         const int ko = koff + 32 * t + 4 * gq, ko2 = ko + 16;
;         const unsigned va = vb_ + (unsigned)(l15 * 128 + (((ko >> 3) ^ vsw) << 4) + ((ko & 4) << 1));
;         const unsigned vh = vb_ + (unsigned)(l15 * 128 + (((ko2 >> 3) ^ vsw) << 4) + ((ko2 & 4) << 1));
; #pragma unroll
;         for (int df = 0; df < 4; ++df) { AT_DSR64(vlo[t][df], va, df * 2048); AT_DSR64(vhi[t][df], vh, df * 2048); }
;     }
;     if (MODE == 2) AT_LW(NKF * 4);
;     bf16x8 pb[NQ][NKF / 2];
; #pragma unroll
;     for (int q = 0; q < NQ; ++q) {
;         unsigned ub = 0; unsigned qm = 0xFFFFFFFFu;
;         if (MODE == 1) ub = (unsigned)((qpos0 + q * 16) - (kpos0 + gq * 4) + 128);
;         if (MODE == 2) qm = ((kpos0 >> q) & 1) ? 0xFFFFFFFFu : 0u;
; #pragma unroll
;         for (int kf = 0; kf < NKF; ++kf)
; #pragma unroll
;             for (int r = 0; r < 4; ++r) {
;                 float xv = __builtin_fmaf(s[q][kf][r], C2, MODE == 2 ? bv[q][kf * 4 + r] : negM2);
;                 if (MODE == 1) { const bool valid = (ub - (unsigned)(kf * 16 + r)) <= 256u; xv = valid ? xv : -1e30f; }
;                 s[q][kf][r] = __builtin_amdgcn_exp2f(xv);
;             }
; template <bool ISA>
; __device__ __forceinline__ void attn_unit(const Params& p, unsigned char* smem, int b, int hh, int blk) {
;     ...
;             if (ISA) {
;                 const bool skip = (t0 > qt0 + 31 + 128) || (t0 + 63 < qt0 - 128);
;                 const bool inner = (t0 >= qt0 + 31 - 128) && (t0 + 63 <= qt0 + 128);
;                 if (inner) attn_tile<NQ, 4, 0>(kb_, vb_, 0, qf, osum, o, l15, gq, 0, 0, negM2, nc);
;                 else if (!skip) attn_tile<NQ, 4, 1>(kb_, vb_, 0, qf, osum, o, l15, gq, qt0 + l15, t0, negM2, nc);
.LBB0_413:
	s_or_saveexec_b64 s[60:61], s[0:1]
	s_nop 1
	s_xor_b64 exec, exec, s[60:61]
	s_cbranch_execz .LBB0_404
	v_cmp_lt_i32_e64 s[0:1], v86, v105
	v_cmp_gt_i32_e64 s[6:7], v86, v106
	s_or_b64 s[0:1], s[0:1], s[6:7]
	s_and_saveexec_b64 s[6:7], s[0:1]
	s_xor_b64 s[64:65], exec, s[6:7]
	s_cbranch_execz .LBB0_418
	v_add_u32_e32 v70, 63, v86
	v_cmp_le_i32_e64 s[0:1], v86, v107
	v_cmp_ge_i32_e64 s[6:7], v70, v108
	s_and_b64 s[0:1], s[0:1], s[6:7]
	s_and_saveexec_b64 s[40:41], s[0:1]
	s_cbranch_execz .LBB0_417
	v_add_u32_e32 v160, s73, v112
	v_add_u32_e32 v70, v160, v132
	ds_read_b128 v[58:61], v70 offset:0
	ds_read_b128 v[62:65], v70 offset:0x800
	ds_read_b128 v[66:69], v70 offset:0x1000
	ds_read_b128 v[70:73], v70 offset:0x1800
	v_add_u32_e32 v131, v160, v131
	ds_read_b128 v[74:77], v131 offset:0
	ds_read_b128 v[78:81], v131 offset:0x800
	ds_read_b128 v[132:135], v131 offset:0x1000
	ds_read_b128 v[136:139], v131 offset:0x1800
	s_nop 0
	s_waitcnt lgkmcnt(7)
	v_mfma_f32_16x16x32_bf16 v[140:143], v[58:61], v[14:17], 0
	v_mfma_f32_16x16x32_bf16 v[58:61], v[58:61], v[6:9], 0
	s_waitcnt lgkmcnt(6)
	v_mfma_f32_16x16x32_bf16 v[144:147], v[62:65], v[14:17], 0
	v_mfma_f32_16x16x32_bf16 v[62:65], v[62:65], v[6:9], 0
	s_waitcnt lgkmcnt(5)
	v_mfma_f32_16x16x32_bf16 v[148:151], v[66:69], v[14:17], 0
	v_mfma_f32_16x16x32_bf16 v[66:69], v[66:69], v[6:9], 0
	s_waitcnt lgkmcnt(4)
	v_mfma_f32_16x16x32_bf16 v[152:155], v[70:73], v[14:17], 0
	v_mfma_f32_16x16x32_bf16 v[70:73], v[70:73], v[6:9], 0
	s_waitcnt lgkmcnt(3)
	v_mfma_f32_16x16x32_bf16 v[58:61], v[74:77], v[10:13], v[58:61]
	s_waitcnt lgkmcnt(2)
	v_mfma_f32_16x16x32_bf16 v[62:65], v[78:81], v[10:13], v[62:65]
	s_waitcnt lgkmcnt(1)
	v_mfma_f32_16x16x32_bf16 v[66:69], v[132:135], v[10:13], v[66:69]
	v_mfma_f32_16x16x32_bf16 v[140:143], v[74:77], v[2:5], v[140:143]
	v_mfma_f32_16x16x32_bf16 v[74:77], v[78:81], v[2:5], v[144:147]
	v_mfma_f32_16x16x32_bf16 v[78:81], v[132:135], v[2:5], v[148:151]
	s_waitcnt lgkmcnt(0)
	v_mfma_f32_16x16x32_bf16 v[132:135], v[136:139], v[2:5], v[152:155]
	v_mfma_f32_16x16x32_bf16 v[136:139], v[136:139], v[10:13], v[70:73]
	s_nop 2
	v_add_u32_e32 v70, v160, v129
	v_add_u32_e32 v71, v160, v130
	ds_read_b64 v[144:145], v70 offset:0
	ds_read_b64 v[146:147], v71 offset:0
	ds_read_b64 v[148:149], v70 offset:0x800
	ds_read_b64 v[150:151], v71 offset:0x800
	ds_read_b64 v[152:153], v70 offset:0x1000
	ds_read_b64 v[154:155], v71 offset:0x1000
	ds_read_b64 v[156:157], v70 offset:0x1800
	v_add_u32_e32 v70, v160, v127
	v_fma_f32 v127, v140, s63, -v100
	v_add_u32_e32 v140, -16, v110
	v_cmp_gt_u32_e64 s[0:1], s62, v140
	v_fma_f32 v140, v141, s63, -v100
	v_subrev_u32_e32 v141, 17, v110
	v_cmp_gt_u32_e64 s[6:7], s62, v141
	v_fma_f32 v141, v142, s63, -v100
	v_subrev_u32_e32 v142, 18, v110
	v_cmp_gt_u32_e64 s[8:9], s62, v142
	v_fma_f32 v142, v143, s63, -v100
	v_subrev_u32_e32 v143, 19, v110
	v_cmp_gt_u32_e64 s[10:11], s62, v143
	v_subrev_u32_e32 v143, 32, v110
	v_fma_f32 v74, v74, s63, -v100
	v_cmp_gt_u32_e64 s[12:13], s62, v143
	v_cndmask_b32_e64 v127, v124, v127, s[0:1]
	v_cndmask_b32_e64 v140, v124, v140, s[6:7]
	v_cndmask_b32_e64 v74, v124, v74, s[12:13]
	v_exp_f32_e32 v143, v74
	v_fma_f32 v74, v75, s63, -v100
	v_subrev_u32_e32 v75, 33, v110
	v_cmp_gt_u32_e64 s[14:15], s62, v75
	v_subrev_u32_e32 v75, 34, v110
	v_cmp_gt_u32_e64 s[16:17], s62, v75
	v_cndmask_b32_e64 v74, v124, v74, s[14:15]
	v_exp_f32_e32 v168, v74
	v_fma_f32 v74, v76, s63, -v100
	v_cndmask_b32_e64 v74, v124, v74, s[16:17]
	v_subrev_u32_e32 v75, 35, v110
	v_exp_f32_e32 v169, v74
	v_fma_f32 v74, v77, s63, -v100
	v_cmp_gt_u32_e64 s[18:19], s62, v75
	v_subrev_u32_e32 v75, 48, v110
	v_cmp_gt_u32_e64 s[20:21], s62, v75
	v_cndmask_b32_e64 v74, v124, v74, s[18:19]
	v_exp_f32_e32 v77, v74
	v_fma_f32 v74, v78, s63, -v100
	v_cndmask_b32_e64 v74, v124, v74, s[20:21]
	v_subrev_u32_e32 v75, 49, v110
	v_exp_f32_e32 v78, v74
	v_fma_f32 v74, v79, s63, -v100
	v_cmp_gt_u32_e64 s[22:23], s62, v75
	v_subrev_u32_e32 v75, 50, v110
	v_cmp_gt_u32_e64 s[24:25], s62, v75
	v_cndmask_b32_e64 v74, v124, v74, s[22:23]
	v_exp_f32_e32 v79, v74
	v_fma_f32 v74, v80, s63, -v100
	v_cndmask_b32_e64 v74, v124, v74, s[24:25]
	v_subrev_u32_e32 v75, 51, v110
	v_exp_f32_e32 v80, v74
	v_fma_f32 v74, v81, s63, -v100
	v_cmp_gt_u32_e64 s[26:27], s62, v75
	v_subrev_u32_e32 v75, 64, v110
	v_cmp_gt_u32_e64 s[28:29], s62, v75
	v_cndmask_b32_e64 v74, v124, v74, s[26:27]
	v_exp_f32_e32 v81, v74
	v_fma_f32 v74, v132, s63, -v100
	v_cndmask_b32_e64 v74, v124, v74, s[28:29]
	v_add_u32_e32 v75, 0xffffffbf, v110
	v_exp_f32_e32 v132, v74
	v_fma_f32 v74, v133, s63, -v100
	v_cmp_gt_u32_e64 s[28:29], s62, v75
	v_add_u32_e32 v75, 0xffffffbe, v110
	v_exp_f32_e32 v127, v127
	v_cndmask_b32_e64 v74, v124, v74, s[28:29]
	v_exp_f32_e32 v133, v74
; __device__ __forceinline__ f32x4 mfma16(bf16x8 a, bf16x8 b, f32x4 c) { return __builtin_amdgcn_mfma_f32_16x16x32_bf16(a, b, c, 0, 0, 0); }
; #define AT_LW(n) do { asm volatile("s_waitcnt lgkmcnt(%0)" :: "n"(n) : "memory"); __builtin_amdgcn_sched_barrier(0); } while (0)
; template <int NQ, int NKF, int MODE> ...
;     ...
;         for (int kf = 0; kf < NKF; ++kf)
; #pragma unroll
;             for (int r = 0; r < 4; ++r) {
;                 float xv = __builtin_fmaf(s[q][kf][r], C2, MODE == 2 ? bv[q][kf * 4 + r] : negM2);
;                 if (MODE == 1) { const bool valid = (ub - (unsigned)(kf * 16 + r)) <= 256u; xv = valid ? xv : -1e30f; }
;                 s[q][kf][r] = __builtin_amdgcn_exp2f(xv);
;             }
; #pragma unroll
;         for (int t = 0; t < NKF / 2; ++t) {
;             uint4 w; w.x = pack2(s[q][2 * t][0], s[q][2 * t][1]); w.y = pack2(s[q][2 * t][2], s[q][2 * t][3]);
;             w.z = pack2(s[q][2 * t + 1][0], s[q][2 * t + 1][1]); w.w = pack2(s[q][2 * t + 1][2], s[q][2 * t + 1][3]);
;             if (MODE == 2) { w.x &= nc.cm[0] & qm; w.y &= nc.cm[1] & qm; w.z &= nc.cm[2] & qm; w.w &= nc.cm[3] & qm; }
;             pb[q][t] = __builtin_bit_cast(bf16x8, w);
;         }
;     }
;     const bf16x8 ones = {0x3F80, 0x3F80, 0x3F80, 0x3F80, 0x3F80, 0x3F80, 0x3F80, 0x3F80};
;     AT_LW(0);
; #pragma unroll
;     for (int t = 0; t < NKF / 2; ++t) {
; #pragma unroll
;         for (int q = 0; q < NQ; ++q) osum[q] = mfma16(ones, pb[q][t], osum[q]);
; #pragma unroll
;         for (int df = 0; df < 4; ++df) {
;             const bf16x8 vfr = __builtin_bit_cast(bf16x8, __builtin_shufflevector(vlo[t][df], vhi[t][df], 0, 1, 2, 3));
; #pragma unroll
;             for (int q = 0; q < NQ; ++q) o[q][df] = mfma16(vfr, pb[q][t], o[q][df]);
;         }
	v_fma_f32 v74, v134, s63, -v100
	v_cmp_gt_u32_e64 s[28:29], s62, v75
	v_add_u32_e32 v75, 0xffffffbd, v110
	v_exp_f32_e32 v140, v140
	v_cndmask_b32_e64 v74, v124, v74, s[28:29]
	v_exp_f32_e32 v134, v74
	v_fma_f32 v74, v135, s63, -v100
	v_cmp_gt_u32_e64 s[28:29], s62, v75
	v_cvt_pk_bf16_f32 v78, v78, v79
	v_cvt_pk_bf16_f32 v79, v80, v81
	v_cndmask_b32_e64 v74, v124, v74, s[28:29]
	v_exp_f32_e32 v135, v74
	v_cvt_pk_bf16_f32 v74, v127, v140
	v_cvt_pk_bf16_f32 v80, v132, v133
	v_fma_f32 v58, v58, s63, -v100
	v_cmp_gt_u32_e64 s[28:29], s62, v110
	v_add_u32_e32 v127, -1, v110
	v_fma_f32 v132, v137, s63, -v100
	v_cndmask_b32_e64 v58, v124, v58, s[28:29]
	v_fma_f32 v59, v59, s63, -v100
	v_cmp_gt_u32_e64 s[28:29], s62, v127
	v_add_u32_e32 v127, -2, v110
	v_cndmask_b32_e64 v132, v124, v132, s[22:23]
	v_cvt_pk_bf16_f32 v81, v134, v135
	v_cndmask_b32_e64 v59, v124, v59, s[28:29]
	v_fma_f32 v60, v60, s63, -v100
	v_cmp_gt_u32_e64 s[28:29], s62, v127
	v_add_u32_e32 v127, -3, v110
	v_exp_f32_e32 v134, v132
	v_fma_f32 v132, v138, s63, -v100
	v_cndmask_b32_e64 v60, v124, v60, s[28:29]
	v_fma_f32 v61, v61, s63, -v100
	v_cmp_gt_u32_e64 s[28:29], s62, v127
	v_fma_f32 v62, v62, s63, -v100
	v_fma_f32 v63, v63, s63, -v100
	v_fma_f32 v64, v64, s63, -v100
	v_fma_f32 v65, v65, s63, -v100
	v_cndmask_b32_e64 v132, v124, v132, s[24:25]
	v_cndmask_b32_e64 v61, v124, v61, s[28:29]
	v_cndmask_b32_e64 v62, v124, v62, s[0:1]
	v_cndmask_b32_e64 v63, v124, v63, s[6:7]
	v_cndmask_b32_e64 v64, v124, v64, s[8:9]
	v_cndmask_b32_e64 v65, v124, v65, s[10:11]
	v_fma_f32 v66, v66, s63, -v100
	v_fma_f32 v67, v67, s63, -v100
	v_fma_f32 v68, v68, s63, -v100
	v_fma_f32 v69, v69, s63, -v100
	v_fma_f32 v127, v136, s63, -v100
	v_exp_f32_e32 v135, v132
	v_fma_f32 v132, v139, s63, -v100
	v_cndmask_b32_e64 v141, v124, v141, s[8:9]
	v_cndmask_b32_e64 v142, v124, v142, s[10:11]
	v_exp_f32_e32 v58, v58
	v_exp_f32_e32 v59, v59
	v_exp_f32_e32 v60, v60
	v_exp_f32_e32 v61, v61
	v_exp_f32_e32 v62, v62
	v_exp_f32_e32 v63, v63
	v_exp_f32_e32 v64, v64
	v_exp_f32_e32 v65, v65
	v_cndmask_b32_e64 v66, v124, v66, s[12:13]
	v_cndmask_b32_e64 v67, v124, v67, s[14:15]
	v_cndmask_b32_e64 v68, v124, v68, s[16:17]
	v_cndmask_b32_e64 v69, v124, v69, s[18:19]
	v_cndmask_b32_e64 v127, v124, v127, s[20:21]
	v_cndmask_b32_e64 v132, v124, v132, s[26:27]
	v_add_u32_e32 v72, v160, v128
	v_exp_f32_e32 v141, v141
	v_exp_f32_e32 v142, v142
	v_exp_f32_e32 v66, v66
	v_exp_f32_e32 v67, v67
	v_exp_f32_e32 v68, v68
	v_exp_f32_e32 v69, v69
	v_exp_f32_e32 v127, v127
	v_exp_f32_e32 v136, v132
	ds_read_b64 v[158:159], v71 offset:0x1800
	ds_read_b64 v[128:129], v70 offset:0
	ds_read_b64 v[130:131], v72 offset:0
	ds_read_b64 v[160:161], v70 offset:0x800
	ds_read_b64 v[162:163], v72 offset:0x800
	ds_read_b64 v[164:165], v70 offset:0x1000
	ds_read_b64 v[166:167], v72 offset:0x1000
	ds_read_b64 v[70:71], v70 offset:0x1800
	ds_read_b64 v[72:73], v72 offset:0x1800
	s_waitcnt lgkmcnt(0)
	v_cvt_pk_bf16_f32 v58, v58, v59
	v_cvt_pk_bf16_f32 v59, v60, v61
	v_cvt_pk_bf16_f32 v60, v62, v63
	v_cvt_pk_bf16_f32 v61, v64, v65
	v_cvt_pk_bf16_f32 v75, v141, v142
	v_cvt_pk_bf16_f32 v76, v143, v168
	v_cvt_pk_bf16_f32 v77, v169, v77
	v_cvt_pk_bf16_f32 v132, v66, v67
	v_cvt_pk_bf16_f32 v133, v68, v69
	v_cvt_pk_bf16_f32 v134, v127, v134
	v_cvt_pk_bf16_f32 v135, v135, v136
	s_mov_b32 s38, s36
	s_mov_b32 s39, s36
	s_mov_b32 s37, s36
	v_mov_b64_e32 v[64:65], s[38:39]
	v_mov_b64_e32 v[62:63], s[36:37]
	v_mfma_f32_16x16x32_bf16 v[54:57], v[144:147], v[74:77], v[54:57]
	v_mfma_f32_16x16x32_bf16 v[50:53], v[144:147], v[58:61], v[50:53]
	v_mfma_f32_16x16x32_bf16 v[46:49], v[148:151], v[74:77], v[46:49]
	v_mfma_f32_16x16x32_bf16 v[38:41], v[62:65], v[74:77], v[38:41]
	v_mfma_f32_16x16x32_bf16 v[26:29], v[62:65], v[58:61], v[26:29]
	v_mfma_f32_16x16x32_bf16 v[22:25], v[148:151], v[58:61], v[22:25]
	v_mfma_f32_16x16x32_bf16 v[42:45], v[152:155], v[74:77], v[42:45]
	v_mfma_f32_16x16x32_bf16 v[18:21], v[152:155], v[58:61], v[18:21]
	v_mfma_f32_16x16x32_bf16 v[34:37], v[156:159], v[74:77], v[34:37]
	v_mfma_f32_16x16x32_bf16 v[30:33], v[156:159], v[58:61], v[30:33]
	v_mfma_f32_16x16x32_bf16 v[54:57], v[128:131], v[78:81], v[54:57]
	v_mfma_f32_16x16x32_bf16 v[50:53], v[128:131], v[132:135], v[50:53]
	v_mfma_f32_16x16x32_bf16 v[46:49], v[160:163], v[78:81], v[46:49]
	v_mfma_f32_16x16x32_bf16 v[38:41], v[62:65], v[78:81], v[38:41]
	v_mfma_f32_16x16x32_bf16 v[26:29], v[62:65], v[132:135], v[26:29]
	v_mfma_f32_16x16x32_bf16 v[22:25], v[160:163], v[132:135], v[22:25]
	v_mfma_f32_16x16x32_bf16 v[42:45], v[164:167], v[78:81], v[42:45]
	v_mfma_f32_16x16x32_bf16 v[18:21], v[164:167], v[132:135], v[18:21]
	v_mfma_f32_16x16x32_bf16 v[34:37], v[70:73], v[78:81], v[34:37]
	v_mfma_f32_16x16x32_bf16 v[30:33], v[70:73], v[132:135], v[30:33]

; template <int NQ, int NKF, int MODE> ...
;     ...
;     for (int ks = 0; ks < 2; ++ks)
; #pragma unroll
;         for (int kf = 0; kf < NKF; ++kf)
; #pragma unroll
;             for (int q = 0; q < NQ; ++q) s[q][kf] = mfma16(kfr[ks][kf], qf[q][ks], s[q][kf]);
;     __builtin_amdgcn_sched_barrier(0);
; #pragma unroll
;     for (int t = 0; t < NKF / 2; ++t) {
;         const int ko = koff + 32 * t + 4 * gq, ko2 = ko + 16;
;         const unsigned va = vb_ + (unsigned)(l15 * 128 + (((ko >> 3) ^ vsw) << 4) + ((ko & 4) << 1));
;         const unsigned vh = vb_ + (unsigned)(l15 * 128 + (((ko2 >> 3) ^ vsw) << 4) + ((ko2 & 4) << 1));
; #pragma unroll
;         for (int df = 0; df < 4; ++df) { AT_DSR64(vlo[t][df], va, df * 2048); AT_DSR64(vhi[t][df], vh, df * 2048); }
;     }
;     if (MODE == 2) AT_LW(NKF * 4);
;     bf16x8 pb[NQ][NKF / 2];
; #pragma unroll
;     for (int q = 0; q < NQ; ++q) {
;         unsigned ub = 0; unsigned qm = 0xFFFFFFFFu;
;         if (MODE == 1) ub = (unsigned)((qpos0 + q * 16) - (kpos0 + gq * 4) + 128);
;         if (MODE == 2) qm = ((kpos0 >> q) & 1) ? 0xFFFFFFFFu : 0u;
; #pragma unroll
;         for (int kf = 0; kf < NKF; ++kf)
; #pragma unroll
;             for (int r = 0; r < 4; ++r) {
;                 float xv = __builtin_fmaf(s[q][kf][r], C2, MODE == 2 ? bv[q][kf * 4 + r] : negM2);
;                 if (MODE == 1) { const bool valid = (ub - (unsigned)(kf * 16 + r)) <= 256u; xv = valid ? xv : -1e30f; }
;                 s[q][kf][r] = __builtin_amdgcn_exp2f(xv);
;             }
; #pragma unroll
;         for (int t = 0; t < NKF / 2; ++t) {
;             uint4 w; w.x = pack2(s[q][2 * t][0], s[q][2 * t][1]); w.y = pack2(s[q][2 * t][2], s[q][2 * t][3]);
;             w.z = pack2(s[q][2 * t + 1][0], s[q][2 * t + 1][1]); w.w = pack2(s[q][2 * t + 1][2], s[q][2 * t + 1][3]);
;             if (MODE == 2) { w.x &= nc.cm[0] & qm; w.y &= nc.cm[1] & qm; w.z &= nc.cm[2] & qm; w.w &= nc.cm[3] & qm; }
;             pb[q][t] = __builtin_bit_cast(bf16x8, w);
;         }
;     }
;     const bf16x8 ones = {0x3F80, 0x3F80, 0x3F80, 0x3F80, 0x3F80, 0x3F80, 0x3F80, 0x3F80};
;     AT_LW(0);
; #pragma unroll
;     for (int t = 0; t < NKF / 2; ++t) {
; #pragma unroll
;         for (int q = 0; q < NQ; ++q) osum[q] = mfma16(ones, pb[q][t], osum[q]);
; #pragma unroll
;         for (int df = 0; df < 4; ++df) {
.LBB0_418:
	s_andn2_saveexec_b64 s[0:1], s[64:65]
	s_cbranch_execz .LBB0_403
	v_add_u32_e32 v156, s73, v112
	v_add_u32_e32 v70, v156, v132
	ds_read_b128 v[58:61], v70 offset:0
	ds_read_b128 v[62:65], v70 offset:0x800
	ds_read_b128 v[66:69], v70 offset:0x1000
	ds_read_b128 v[70:73], v70 offset:0x1800
	v_add_u32_e32 v131, v156, v131
	ds_read_b128 v[74:77], v131 offset:0
	ds_read_b128 v[78:81], v131 offset:0x800
	ds_read_b128 v[132:135], v131 offset:0x1000
	ds_read_b128 v[136:139], v131 offset:0x1800
	s_nop 0
	s_waitcnt lgkmcnt(7)
	v_mfma_f32_16x16x32_bf16 v[140:143], v[58:61], v[14:17], 0
	v_mfma_f32_16x16x32_bf16 v[58:61], v[58:61], v[6:9], 0
	s_waitcnt lgkmcnt(6)
	v_mfma_f32_16x16x32_bf16 v[144:147], v[62:65], v[14:17], 0
	v_mfma_f32_16x16x32_bf16 v[62:65], v[62:65], v[6:9], 0
	s_waitcnt lgkmcnt(5)
	v_mfma_f32_16x16x32_bf16 v[148:151], v[66:69], v[14:17], 0
	v_mfma_f32_16x16x32_bf16 v[66:69], v[66:69], v[6:9], 0
	s_waitcnt lgkmcnt(4)
	v_mfma_f32_16x16x32_bf16 v[152:155], v[70:73], v[14:17], 0
	v_mfma_f32_16x16x32_bf16 v[70:73], v[70:73], v[6:9], 0
	s_waitcnt lgkmcnt(3)
	v_mfma_f32_16x16x32_bf16 v[58:61], v[74:77], v[10:13], v[58:61]
	s_waitcnt lgkmcnt(2)
	v_mfma_f32_16x16x32_bf16 v[62:65], v[78:81], v[10:13], v[62:65]
	s_waitcnt lgkmcnt(1)
	v_mfma_f32_16x16x32_bf16 v[66:69], v[132:135], v[10:13], v[66:69]
	v_mfma_f32_16x16x32_bf16 v[140:143], v[74:77], v[2:5], v[140:143]
	v_mfma_f32_16x16x32_bf16 v[74:77], v[78:81], v[2:5], v[144:147]
	v_mfma_f32_16x16x32_bf16 v[78:81], v[132:135], v[2:5], v[148:151]
	s_waitcnt lgkmcnt(0)
	v_mfma_f32_16x16x32_bf16 v[132:135], v[136:139], v[2:5], v[152:155]
	v_mfma_f32_16x16x32_bf16 v[70:73], v[136:139], v[10:13], v[70:73]
	v_add_u32_e32 v129, v156, v129
	v_add_u32_e32 v130, v156, v130
	v_add_u32_e32 v127, v156, v127
	s_nop 1
	v_fma_f32 v74, v74, s63, -v100
	ds_read_b64 v[136:137], v129 offset:0
	ds_read_b64 v[138:139], v130 offset:0
	ds_read_b64 v[144:145], v129 offset:0x800
	ds_read_b64 v[146:147], v130 offset:0x800
	ds_read_b64 v[148:149], v129 offset:0x1000
	ds_read_b64 v[150:151], v130 offset:0x1000
	ds_read_b64 v[152:153], v129 offset:0x1800
	ds_read_b64 v[154:155], v130 offset:0x1800
	v_add_u32_e32 v166, v156, v128
	ds_read_b64 v[128:129], v127 offset:0
	ds_read_b64 v[130:131], v166 offset:0
	ds_read_b64 v[156:157], v127 offset:0x800
	ds_read_b64 v[158:159], v166 offset:0x800
	ds_read_b64 v[160:161], v127 offset:0x1000
	ds_read_b64 v[162:163], v166 offset:0x1000
	ds_read_b64 v[164:165], v127 offset:0x1800
	v_fma_f32 v127, v140, s63, -v100
	v_fma_f32 v140, v141, s63, -v100
	v_fma_f32 v141, v142, s63, -v100
	v_fma_f32 v142, v143, s63, -v100
	v_exp_f32_e32 v143, v74
	v_fma_f32 v74, v75, s63, -v100
	v_exp_f32_e32 v168, v74
	v_fma_f32 v74, v76, s63, -v100
	v_exp_f32_e32 v169, v74
	v_fma_f32 v74, v77, s63, -v100
	v_exp_f32_e32 v77, v74
	v_fma_f32 v74, v78, s63, -v100
	v_exp_f32_e32 v78, v74
	v_fma_f32 v74, v79, s63, -v100
	v_exp_f32_e32 v79, v74
	v_fma_f32 v74, v80, s63, -v100
	v_exp_f32_e32 v80, v74
	v_fma_f32 v74, v81, s63, -v100
	v_exp_f32_e32 v81, v74
	v_fma_f32 v74, v132, s63, -v100
	v_exp_f32_e32 v127, v127
	v_exp_f32_e32 v140, v140
	v_exp_f32_e32 v132, v74
	v_fma_f32 v74, v133, s63, -v100
	v_exp_f32_e32 v133, v74
	v_fma_f32 v74, v134, s63, -v100
	v_exp_f32_e32 v134, v74
	v_fma_f32 v74, v135, s63, -v100
	v_fma_f32 v70, v70, s63, -v100
	v_exp_f32_e32 v135, v74
	v_cvt_pk_bf16_f32 v74, v127, v140
	v_exp_f32_e32 v127, v70
	v_fma_f32 v70, v71, s63, -v100
	v_cvt_pk_bf16_f32 v78, v78, v79
	v_cvt_pk_bf16_f32 v79, v80, v81
	v_cvt_pk_bf16_f32 v80, v132, v133
	v_fma_f32 v58, v58, s63, -v100
	v_fma_f32 v59, v59, s63, -v100
	v_fma_f32 v60, v60, s63, -v100
	v_fma_f32 v61, v61, s63, -v100
	v_fma_f32 v62, v62, s63, -v100
	v_fma_f32 v63, v63, s63, -v100
	v_fma_f32 v64, v64, s63, -v100
	v_fma_f32 v65, v65, s63, -v100
	v_exp_f32_e32 v132, v70
	v_fma_f32 v70, v72, s63, -v100
	v_exp_f32_e32 v58, v58
	v_exp_f32_e32 v59, v59
	v_exp_f32_e32 v60, v60
	v_exp_f32_e32 v61, v61
	v_exp_f32_e32 v62, v62
	v_exp_f32_e32 v63, v63
	v_exp_f32_e32 v64, v64
	v_exp_f32_e32 v65, v65
	v_fma_f32 v66, v66, s63, -v100
	v_fma_f32 v67, v67, s63, -v100
	v_fma_f32 v68, v68, s63, -v100
	v_fma_f32 v69, v69, s63, -v100
	v_exp_f32_e32 v133, v70
	v_fma_f32 v70, v73, s63, -v100
	v_exp_f32_e32 v141, v141
	v_exp_f32_e32 v142, v142
	v_exp_f32_e32 v66, v66
	v_exp_f32_e32 v67, v67
	v_exp_f32_e32 v68, v68
	v_exp_f32_e32 v69, v69
	v_exp_f32_e32 v73, v70
	ds_read_b64 v[166:167], v166 offset:0x1800
	s_waitcnt lgkmcnt(0)
	v_cvt_pk_bf16_f32 v58, v58, v59
	v_cvt_pk_bf16_f32 v59, v60, v61
	v_cvt_pk_bf16_f32 v60, v62, v63
	v_cvt_pk_bf16_f32 v61, v64, v65
	v_cvt_pk_bf16_f32 v75, v141, v142
	v_cvt_pk_bf16_f32 v76, v143, v168
	v_cvt_pk_bf16_f32 v77, v169, v77
	v_cvt_pk_bf16_f32 v81, v134, v135
	v_cvt_pk_bf16_f32 v70, v66, v67
	v_cvt_pk_bf16_f32 v71, v68, v69
	v_cvt_pk_bf16_f32 v72, v127, v132
	v_cvt_pk_bf16_f32 v73, v133, v73
	s_mov_b32 s38, s36
	s_mov_b32 s39, s36
	s_mov_b32 s37, s36
	v_mov_b64_e32 v[64:65], s[38:39]
	v_mov_b64_e32 v[62:63], s[36:37]
	v_mfma_f32_16x16x32_bf16 v[54:57], v[136:139], v[74:77], v[54:57]
	v_mfma_f32_16x16x32_bf16 v[50:53], v[136:139], v[58:61], v[50:53]
	v_mfma_f32_16x16x32_bf16 v[46:49], v[144:147], v[74:77], v[46:49]
	v_mfma_f32_16x16x32_bf16 v[38:41], v[62:65], v[74:77], v[38:41]
	v_mfma_f32_16x16x32_bf16 v[26:29], v[62:65], v[58:61], v[26:29]
	v_mfma_f32_16x16x32_bf16 v[22:25], v[144:147], v[58:61], v[22:25]
	v_mfma_f32_16x16x32_bf16 v[42:45], v[148:151], v[74:77], v[42:45]
	v_mfma_f32_16x16x32_bf16 v[18:21], v[148:151], v[58:61], v[18:21]
	v_mfma_f32_16x16x32_bf16 v[34:37], v[152:155], v[74:77], v[34:37]
	v_mfma_f32_16x16x32_bf16 v[30:33], v[152:155], v[58:61], v[30:33]
	v_mfma_f32_16x16x32_bf16 v[54:57], v[128:131], v[78:81], v[54:57]
	v_mfma_f32_16x16x32_bf16 v[50:53], v[128:131], v[70:73], v[50:53]
	v_mfma_f32_16x16x32_bf16 v[46:49], v[156:159], v[78:81], v[46:49]
	v_mfma_f32_16x16x32_bf16 v[38:41], v[62:65], v[78:81], v[38:41]
	v_mfma_f32_16x16x32_bf16 v[26:29], v[62:65], v[70:73], v[26:29]
	v_mfma_f32_16x16x32_bf16 v[22:25], v[156:159], v[70:73], v[22:25]
	v_mfma_f32_16x16x32_bf16 v[42:45], v[160:163], v[78:81], v[42:45]
	v_mfma_f32_16x16x32_bf16 v[18:21], v[160:163], v[70:73], v[18:21]
	v_mfma_f32_16x16x32_bf16 v[34:37], v[164:167], v[78:81], v[34:37]
	v_mfma_f32_16x16x32_bf16 v[30:33], v[164:167], v[70:73], v[30:33]
	s_branch .LBB0_403
; template <bool ISA>
; __device__ __forceinline__ void attn_unit(const Params& p, unsigned char* smem, int b, int hh, int blk) {
;     ...
; #pragma unroll
;     for (int q = 0; q < NQ; ++q) {
;         const float inv = 1.0f / osum[q][0];
;         float ssq = 0.f;
; #pragma unroll
;         for (int df = 0; df < 4; ++df) { o[q][df] *= inv; ssq += o[q][df][0] * o[q][df][0] + o[q][df][1] * o[q][df][1] + o[q][df][2] * o[q][df][2] + o[q][df][3] * o[q][df][3]; }
;         ssq += __shfl_xor(ssq, 16); ssq += __shfl_xor(ssq, 32);
;         const size_t lr = (size_t)b * SEQ + qt0 + q * QSTR + l15;
;         if (gq == 0) p.osq[lr * 16 + (ISA ? hh : 8 + hh)] = ssq;
.LBB0_420:
	s_or_b64 exec, exec, s[82:83]
	s_nop 7
	v_mov_b64_e32 v[66:67], v[54:55]
	v_mov_b64_e32 v[68:69], v[56:57]
	v_mov_b64_e32 v[58:59], v[50:51]
	v_mov_b64_e32 v[60:61], v[52:53]
	v_mov_b64_e32 v[62:63], v[46:47]
	v_mov_b64_e32 v[64:65], v[48:49]
	v_and_b32_e32 v3, 64, v214
	v_xor_b32_e32 v2, 16, v214
	v_add_u32_e32 v3, 64, v3
	v_cmp_lt_i32_e32 vcc, v2, v3
	v_div_scale_f32 v4, s[0:1], v38, v38, 1.0
	s_nop 0
	v_cndmask_b32_e32 v2, v214, v2, vcc
	v_rcp_f32_e32 v5, v4
	v_lshlrev_b32_e32 v40, 2, v2
	v_xor_b32_e32 v2, 32, v214
	v_cmp_lt_i32_e32 vcc, v2, v3
	s_lshl_b32 s76, s5, 13
	v_ashrrev_i32_e32 v85, 31, v84
	v_cndmask_b32_e32 v2, v214, v2, vcc
	v_lshlrev_b32_e32 v41, 2, v2
	v_fma_f32 v2, -v4, v5, 1.0
	v_fmac_f32_e32 v5, v2, v5
	v_div_scale_f32 v2, vcc, 1.0, v38, 1.0
	v_mul_f32_e32 v3, v2, v5
	v_fma_f32 v6, -v4, v3, v2
	v_fmac_f32_e32 v3, v6, v5
	v_fma_f32 v2, -v4, v3, v2
	v_div_fmas_f32 v2, v2, v5, v3
	v_div_fixup_f32 v2, v2, v38, 1.0
	v_pk_mul_f32 v[38:39], v[66:67], v[2:3] op_sel_hi:[1,0]
	v_pk_mul_f32 v[8:9], v[68:69], v[2:3] op_sel_hi:[1,0]
	v_mul_f32_e32 v3, v39, v39
	v_fmac_f32_e32 v3, v38, v38
	v_fmac_f32_e32 v3, v8, v8
	v_fmac_f32_e32 v3, v9, v9
	v_pk_mul_f32 v[28:29], v[62:63], v[2:3] op_sel_hi:[1,0]
	v_pk_mul_f32 v[12:13], v[64:65], v[2:3] op_sel_hi:[1,0]
	v_mul_f32_e32 v4, v29, v29
	v_fmac_f32_e32 v4, v28, v28
	v_fmac_f32_e32 v4, v12, v12
	v_fmac_f32_e32 v4, v13, v13
	v_add_f32_e32 v3, v3, v4
	v_pk_mul_f32 v[16:17], v[42:43], v[2:3] op_sel_hi:[1,0]
	v_pk_mul_f32 v[10:11], v[44:45], v[2:3] op_sel_hi:[1,0]
	v_mul_f32_e32 v4, v17, v17
	v_fmac_f32_e32 v4, v16, v16
	v_fmac_f32_e32 v4, v10, v10
	v_fmac_f32_e32 v4, v11, v11
	v_add_f32_e32 v3, v4, v3
	v_pk_mul_f32 v[14:15], v[34:35], v[2:3] op_sel_hi:[1,0]
	v_pk_mul_f32 v[6:7], v[36:37], v[2:3] op_sel_hi:[1,0]
	v_mul_f32_e32 v2, v15, v15
	v_fmac_f32_e32 v2, v14, v14
	v_fmac_f32_e32 v2, v6, v6
	v_fmac_f32_e32 v2, v7, v7
	v_add_f32_e32 v4, v2, v3
	ds_bpermute_b32 v5, v40, v4
	v_lshl_add_u64 v[2:3], v[84:85], 0, s[76:77]
	v_or_b32_e32 v2, v2, v83
	v_cmp_gt_u32_e64 s[0:1], 16, v87
	s_waitcnt lgkmcnt(0)
	v_add_f32_e32 v27, v4, v5
	ds_bpermute_b32 v34, v41, v27
	v_lshlrev_b32_e32 v4, 2, v82
	v_mov_b32_e32 v5, v99
	v_lshl_add_u64 v[4:5], s[70:71], 0, v[4:5]
	s_and_saveexec_b64 s[6:7], s[0:1]
	s_cbranch_execz .LBB0_422
	s_waitcnt lgkmcnt(0)
	v_add_f32_e32 v27, v27, v34
	v_lshlrev_b64 v[34:35], 6, v[2:3]
	v_lshl_add_u64 v[34:35], v[4:5], 0, v[34:35]
	global_store_dword v[34:35], v27, off
